# loop edge: out-/down-projection K-loop issues its first eight LDS reads before the per-iteration scalar preamble (plane pointer arithmetic)
# baseline (speedup 1.0000x reference)
; #define PG8_STAGE(bufoff, gbase, voff) do { _Pragma("unroll") for (int _i = 0; _i < 2; ++_i) \
;         __builtin_amdgcn_global_load_lds((const unsigned*)((const char*)(gbase) + (voff)[_i]), (PG8_LAS unsigned*)(lds + (bufoff) + ldsw + _i * 8192), 16, 0, 0); } while (0)
; #define PG8_LDA(dst, b, h) do { _Pragma("unroll") for (int m = 0; m < 4; ++m) _Pragma("unroll") for (int k = 0; k < 2; ++k) dst[m][k] = *(const PG8_LAS bf16x8*)(lds + PG8_SA(b, h) + aoff + m * 2048 + k * 1024); } while (0)
; #define PG8_LDB(dst, b, h) do { _Pragma("unroll") for (int n = 0; n < 2; ++n) _Pragma("unroll") for (int k = 0; k < 2; ++k) dst[n][k] = *(const PG8_LAS bf16x8*)(lds + PG8_SB(b, h) + boff + n * 2048 + k * 1024); } while (0)
; #define PG8_MMA(ai, bj, At, Bt) do { __builtin_amdgcn_s_setprio(1); _Pragma("unroll") for (int m = 0; m < 4; ++m) _Pragma("unroll") for (int n = 0; n < 2; ++n) _Pragma("unroll") for (int k = 0; k < 2; ++k) \
;         acc[ai][bj][m][n] = __builtin_amdgcn_mfma_f32_16x16x32_bf16(Bt[n][k], At[m][k], acc[ai][bj][m][n], 0, 0, 0); __builtin_amdgcn_s_setprio(0); } while (0)
; #define PG8_WAIT_V(n) asm volatile("s_waitcnt vmcnt(" #n ")" ::: "memory")
; #define PG8_WAIT_L(n) asm volatile("s_waitcnt lgkmcnt(" #n ")" ::: "memory")
; #define PG8_BAR __builtin_amdgcn_s_barrier()
; #define PG8_SCHED __builtin_amdgcn_sched_barrier(0)
; template <class Epi, class Sched, bool ALIGN_EPI = false, bool SP2 = false>
; __device__ __forceinline__ void gemm_phase(PG8_LAS unsigned char* lds, const Gemm g, const Sched& S, const Epi& E, const int tid) {
;     ...
;             PG8_LDB(B0, 0, 0); PG8_LDB(B1, 0, 1); PG8_SCHED; PG8_LDA(At, 0, 0); PG8_STAGE(PG8_SA(1, 1), a1 + hstepA, voffA);
;             PG8_WAIT_V(8); PG8_WAIT_L(0); PG8_BAR; PG8_MMA(0, 0, At, B0); PG8_MMA(0, 1, At, B1); PG8_BAR; PG8_SCHED;
;             PG8_LDA(At, 0, 1); PG8_STAGE(PG8_SB(0, 0), b2, voffB); PG8_STAGE(PG8_SB(0, 1), b2 + hstep, voffB); PG8_STAGE(PG8_SA(0, 0), a2, voffA);
;             PG8_WAIT_V(8); PG8_WAIT_L(0); PG8_BAR; PG8_MMA(1, 0, At, B0); PG8_MMA(1, 1, At, B1); PG8_BAR; PG8_SCHED;
.LBB0_416:
	s_lshr_b64 s[68:69], s[28:29], 4
	v_mad_u64_u32 v[190:191], s[70:71], s68, v227, v[74:75]
	s_lshr_b32 s69, s29, 4
	s_mul_i32 s70, s69, 0x7ff800
	v_mad_u64_u32 v[222:223], s[68:69], s68, v227, v[76:77]
	s_add_u32 s68, s19, s30
	s_addc_u32 s69, s65, s31
	s_and_b64 s[40:41], exec, s[40:41]
	v_add_u32_e32 v191, s70, v191
	v_add_u32_e32 v223, s70, v223
	s_cselect_b32 s41, s1, s69
	s_cselect_b32 s40, s17, s68
	v_lshl_add_u64 v[222:223], v[222:223], 0, s[30:31]
	s_add_i32 m0, s47, 0xc000
	ds_read_b128 v[166:169], v208
	ds_read_b128 v[170:173], v208 offset:1024
	ds_read_b128 v[174:177], v208 offset:2048
	ds_read_b128 v[178:181], v208 offset:3072
	ds_read_b128 v[182:185], v208 offset:4096
	ds_read_b128 v[186:189], v208 offset:5120
	ds_read_b128 v[218:221], v208 offset:6144
	ds_read_b128 v[234:237], v208 offset:7168
	global_load_lds_dwordx4 v[222:223], off
	v_lshl_add_u64 v[190:191], v[190:191], 0, s[30:31]
	s_add_i32 m0, s47, 0xe000
	s_nop 0
	global_load_lds_dwordx4 v[190:191], off
	s_waitcnt vmcnt(8)
	s_waitcnt lgkmcnt(0)
	s_barrier
	s_setprio 1
	s_waitcnt lgkmcnt(0)
	v_mfma_f32_16x16x32_bf16 v[162:165], v[86:89], v[166:169], v[162:165]
	v_mfma_f32_16x16x32_bf16 v[158:161], v[106:109], v[166:169], v[158:161]
	v_mfma_f32_16x16x32_bf16 v[134:137], v[86:89], v[174:177], v[134:137]
	v_mfma_f32_16x16x32_bf16 v[130:133], v[106:109], v[174:177], v[130:133]
	v_mfma_f32_16x16x32_bf16 v[110:113], v[86:89], v[182:185], v[110:113]
	v_mfma_f32_16x16x32_bf16 v[102:105], v[106:109], v[182:185], v[102:105]
	v_mfma_f32_16x16x32_bf16 v[82:85], v[86:89], v[218:221], v[82:85]
	v_mfma_f32_16x16x32_bf16 v[78:81], v[106:109], v[218:221], v[78:81]
	v_mfma_f32_16x16x32_bf16 v[162:165], v[98:101], v[170:173], v[162:165]
	v_mfma_f32_16x16x32_bf16 v[158:161], v[122:125], v[170:173], v[158:161]
	v_mfma_f32_16x16x32_bf16 v[134:137], v[98:101], v[178:181], v[134:137]
	v_mfma_f32_16x16x32_bf16 v[130:133], v[122:125], v[178:181], v[130:133]
	v_mfma_f32_16x16x32_bf16 v[110:113], v[98:101], v[186:189], v[110:113]
	v_mfma_f32_16x16x32_bf16 v[102:105], v[122:125], v[186:189], v[102:105]
	v_mfma_f32_16x16x32_bf16 v[82:85], v[98:101], v[234:237], v[82:85]
	v_mfma_f32_16x16x32_bf16 v[78:81], v[122:125], v[234:237], v[78:81]
	s_setprio 0
	s_setprio 1
	v_mfma_f32_16x16x32_bf16 v[146:149], v[126:129], v[166:169], v[146:149]
	v_mfma_f32_16x16x32_bf16 v[138:141], v[150:153], v[166:169], v[138:141]
	v_mfma_f32_16x16x32_bf16 v[118:121], v[126:129], v[174:177], v[118:121]
	v_mfma_f32_16x16x32_bf16 v[114:117], v[150:153], v[174:177], v[114:117]
	v_mfma_f32_16x16x32_bf16 v[94:97], v[126:129], v[182:185], v[94:97]
	v_mfma_f32_16x16x32_bf16 v[90:93], v[150:153], v[182:185], v[90:93]
	v_mfma_f32_16x16x32_bf16 v[70:73], v[126:129], v[218:221], v[70:73]
	v_mfma_f32_16x16x32_bf16 v[66:69], v[150:153], v[218:221], v[66:69]
	v_mfma_f32_16x16x32_bf16 v[146:149], v[142:145], v[170:173], v[146:149]
	v_mfma_f32_16x16x32_bf16 v[138:141], v[154:157], v[170:173], v[138:141]
	v_mfma_f32_16x16x32_bf16 v[118:121], v[142:145], v[178:181], v[118:121]
	v_mfma_f32_16x16x32_bf16 v[114:117], v[154:157], v[178:181], v[114:117]
	v_mfma_f32_16x16x32_bf16 v[94:97], v[142:145], v[186:189], v[94:97]
	v_mfma_f32_16x16x32_bf16 v[90:93], v[154:157], v[186:189], v[90:93]
	v_mfma_f32_16x16x32_bf16 v[70:73], v[142:145], v[234:237], v[70:73]
	v_mfma_f32_16x16x32_bf16 v[66:69], v[154:157], v[234:237], v[66:69]
	s_setprio 0
	s_barrier
	s_mov_b32 m0, s5
	v_lshl_add_u64 v[190:191], s[40:41], 0, v[198:199]
	v_lshl_add_u64 v[222:223], s[40:41], 0, v[202:203]
	s_add_u32 s40, s40, s46
	ds_read_b128 v[166:169], v208 offset:16384
	ds_read_b128 v[170:173], v208 offset:17408
	ds_read_b128 v[174:177], v208 offset:18432
	ds_read_b128 v[178:181], v208 offset:19456
	ds_read_b128 v[182:185], v208 offset:20480
	ds_read_b128 v[186:189], v208 offset:21504
	ds_read_b128 v[218:221], v208 offset:22528
	ds_read_b128 v[234:237], v208 offset:23552
	global_load_lds_dwordx4 v[190:191], off
	s_mov_b32 m0, s48
	s_addc_u32 s41, s41, 0
	global_load_lds_dwordx4 v[222:223], off
	v_lshl_add_u64 v[228:229], s[40:41], 0, v[198:199]
	s_mov_b32 m0, s49
	v_lshl_add_u64 v[240:241], s[40:41], 0, v[202:203]
	global_load_lds_dwordx4 v[228:229], off
	s_mov_b32 m0, s50
	v_lshl_add_u64 v[242:243], s[38:39], 0, v[196:197]
	global_load_lds_dwordx4 v[240:241], off
	s_mov_b32 m0, s47
	v_lshl_add_u64 v[244:245], s[38:39], 0, v[200:201]
	global_load_lds_dwordx4 v[242:243], off
	s_mov_b32 m0, s51
	s_nop 0
	global_load_lds_dwordx4 v[244:245], off
	s_waitcnt vmcnt(8)
	s_waitcnt lgkmcnt(0)
	s_barrier
; #define PG8_STAGE(bufoff, gbase, voff) do { _Pragma("unroll") for (int _i = 0; _i < 2; ++_i) \
;         __builtin_amdgcn_global_load_lds((const unsigned*)((const char*)(gbase) + (voff)[_i]), (PG8_LAS unsigned*)(lds + (bufoff) + ldsw + _i * 8192), 16, 0, 0); } while (0)
; #define PG8_LDA(dst, b, h) do { _Pragma("unroll") for (int m = 0; m < 4; ++m) _Pragma("unroll") for (int k = 0; k < 2; ++k) dst[m][k] = *(const PG8_LAS bf16x8*)(lds + PG8_SA(b, h) + aoff + m * 2048 + k * 1024); } while (0)
; #define PG8_LDB(dst, b, h) do { _Pragma("unroll") for (int n = 0; n < 2; ++n) _Pragma("unroll") for (int k = 0; k < 2; ++k) dst[n][k] = *(const PG8_LAS bf16x8*)(lds + PG8_SB(b, h) + boff + n * 2048 + k * 1024); } while (0)
; #define PG8_MMA(ai, bj, At, Bt) do { __builtin_amdgcn_s_setprio(1); _Pragma("unroll") for (int m = 0; m < 4; ++m) _Pragma("unroll") for (int n = 0; n < 2; ++n) _Pragma("unroll") for (int k = 0; k < 2; ++k) \
;         acc[ai][bj][m][n] = __builtin_amdgcn_mfma_f32_16x16x32_bf16(Bt[n][k], At[m][k], acc[ai][bj][m][n], 0, 0, 0); __builtin_amdgcn_s_setprio(0); } while (0)
; #define PG8_WAIT_V(n) asm volatile("s_waitcnt vmcnt(" #n ")" ::: "memory")
; #define PG8_WAIT_L(n) asm volatile("s_waitcnt lgkmcnt(" #n ")" ::: "memory")
; #define PG8_BAR __builtin_amdgcn_s_barrier()
; #define PG8_SCHED __builtin_amdgcn_sched_barrier(0)
; template <class Epi, class Sched, bool ALIGN_EPI = false, bool SP2 = false>
; __device__ __forceinline__ void gemm_phase(PG8_LAS unsigned char* lds, const Gemm g, const Sched& S, const Epi& E, const int tid) {
;     ...
;             PG8_WAIT_V(8); PG8_WAIT_L(0); PG8_BAR; PG8_MMA(1, 0, At, B0); PG8_MMA(1, 1, At, B1); PG8_BAR; PG8_SCHED;
;             PG8_LDB(B0, 1, 0); PG8_LDB(B1, 1, 1); PG8_SCHED; PG8_LDA(At, 1, 0); PG8_STAGE(PG8_SA(0, 1), a2 + hstepA, voffA);
;             PG8_WAIT_V(8); PG8_WAIT_L(0); PG8_BAR; PG8_MMA(0, 0, At, B0); PG8_MMA(0, 1, At, B1); PG8_BAR; PG8_SCHED;
;             PG8_LDA(At, 1, 1); PG8_STAGE(PG8_SB(1, 0), b3, voffB); PG8_STAGE(PG8_SB(1, 1), b3 + hstep, voffB); PG8_STAGE(PG8_SA(1, 0), a3, voffA);
	s_setprio 1
	s_waitcnt lgkmcnt(0)
	v_mfma_f32_16x16x32_bf16 v[62:65], v[86:89], v[166:169], v[62:65]
	v_mfma_f32_16x16x32_bf16 v[58:61], v[106:109], v[166:169], v[58:61]
	v_mfma_f32_16x16x32_bf16 v[46:49], v[86:89], v[174:177], v[46:49]
	v_mfma_f32_16x16x32_bf16 v[42:45], v[106:109], v[174:177], v[42:45]
	v_mfma_f32_16x16x32_bf16 v[30:33], v[86:89], v[182:185], v[30:33]
	v_mfma_f32_16x16x32_bf16 v[26:29], v[106:109], v[182:185], v[26:29]
	v_mfma_f32_16x16x32_bf16 v[14:17], v[86:89], v[218:221], v[14:17]
	v_mfma_f32_16x16x32_bf16 v[10:13], v[106:109], v[218:221], v[10:13]
	v_mfma_f32_16x16x32_bf16 v[62:65], v[98:101], v[170:173], v[62:65]
	v_mfma_f32_16x16x32_bf16 v[58:61], v[122:125], v[170:173], v[58:61]
	v_mfma_f32_16x16x32_bf16 v[46:49], v[98:101], v[178:181], v[46:49]
	v_mfma_f32_16x16x32_bf16 v[42:45], v[122:125], v[178:181], v[42:45]
	v_mfma_f32_16x16x32_bf16 v[30:33], v[98:101], v[186:189], v[30:33]
	v_mfma_f32_16x16x32_bf16 v[26:29], v[122:125], v[186:189], v[26:29]
	v_mfma_f32_16x16x32_bf16 v[14:17], v[98:101], v[234:237], v[14:17]
	v_mfma_f32_16x16x32_bf16 v[10:13], v[122:125], v[234:237], v[10:13]
	s_setprio 0
	s_setprio 1
	v_mfma_f32_16x16x32_bf16 v[54:57], v[126:129], v[166:169], v[54:57]
	v_mfma_f32_16x16x32_bf16 v[50:53], v[150:153], v[166:169], v[50:53]
	v_mfma_f32_16x16x32_bf16 v[38:41], v[126:129], v[174:177], v[38:41]
	v_mfma_f32_16x16x32_bf16 v[34:37], v[150:153], v[174:177], v[34:37]
	v_mfma_f32_16x16x32_bf16 v[22:25], v[126:129], v[182:185], v[22:25]
	v_mfma_f32_16x16x32_bf16 v[18:21], v[150:153], v[182:185], v[18:21]
	v_mfma_f32_16x16x32_bf16 v[6:9], v[126:129], v[218:221], v[6:9]
	v_mfma_f32_16x16x32_bf16 v[2:5], v[150:153], v[218:221], v[2:5]
	v_mfma_f32_16x16x32_bf16 v[54:57], v[142:145], v[170:173], v[54:57]
	v_mfma_f32_16x16x32_bf16 v[50:53], v[154:157], v[170:173], v[50:53]
	v_mfma_f32_16x16x32_bf16 v[38:41], v[142:145], v[178:181], v[38:41]
	v_mfma_f32_16x16x32_bf16 v[34:37], v[154:157], v[178:181], v[34:37]
	v_mfma_f32_16x16x32_bf16 v[22:25], v[142:145], v[186:189], v[22:25]
	v_mfma_f32_16x16x32_bf16 v[18:21], v[154:157], v[186:189], v[18:21]
	v_mfma_f32_16x16x32_bf16 v[6:9], v[142:145], v[234:237], v[6:9]
	v_mfma_f32_16x16x32_bf16 v[2:5], v[154:157], v[234:237], v[2:5]
	s_setprio 0
	s_barrier
	v_or_b32_e32 v0, 0x18000, v209
	v_add_u32_e32 v98, 0x18400, v209
	ds_read_b128 v[86:89], v0
	ds_read_b128 v[98:101], v98
	v_add_u32_e32 v0, 0x18800, v209
	v_add_u32_e32 v122, 0x18c00, v209
	ds_read_b128 v[106:109], v0
	ds_read_b128 v[122:125], v122
	v_or_b32_e32 v0, 0x1c000, v209
	v_add_u32_e32 v142, 0x1c400, v209
	ds_read_b128 v[126:129], v0
	ds_read_b128 v[142:145], v142
	v_add_u32_e32 v0, 0x1c800, v209
	v_add_u32_e32 v154, 0x1cc00, v209
	ds_read_b128 v[150:153], v0
	ds_read_b128 v[154:157], v154
	s_add_u32 s38, s38, 0x40000
	s_addc_u32 s39, s39, 0
	s_mov_b32 m0, s52
	v_lshl_add_u64 v[246:247], s[38:39], 0, v[196:197]
	ds_read_b128 v[166:169], v208 offset:32768
	ds_read_b128 v[170:173], v208 offset:33792
	ds_read_b128 v[174:177], v208 offset:34816
	ds_read_b128 v[178:181], v208 offset:35840
	ds_read_b128 v[182:185], v208 offset:36864
	ds_read_b128 v[186:189], v208 offset:37888
	ds_read_b128 v[218:221], v208 offset:38912
	ds_read_b128 v[234:237], v208 offset:39936
	global_load_lds_dwordx4 v[246:247], off
	v_lshl_add_u64 v[246:247], s[38:39], 0, v[200:201]
	s_mov_b32 m0, s53
	s_nop 0
	global_load_lds_dwordx4 v[246:247], off
	s_waitcnt vmcnt(8)
	s_waitcnt lgkmcnt(0)
	s_barrier
	s_setprio 1
	s_waitcnt lgkmcnt(0)
	v_mfma_f32_16x16x32_bf16 v[162:165], v[86:89], v[166:169], v[162:165]
	v_mfma_f32_16x16x32_bf16 v[158:161], v[106:109], v[166:169], v[158:161]
	v_mfma_f32_16x16x32_bf16 v[134:137], v[86:89], v[174:177], v[134:137]
	v_mfma_f32_16x16x32_bf16 v[130:133], v[106:109], v[174:177], v[130:133]
	v_mfma_f32_16x16x32_bf16 v[110:113], v[86:89], v[182:185], v[110:113]
	v_mfma_f32_16x16x32_bf16 v[102:105], v[106:109], v[182:185], v[102:105]
	v_mfma_f32_16x16x32_bf16 v[82:85], v[86:89], v[218:221], v[82:85]
	v_mfma_f32_16x16x32_bf16 v[78:81], v[106:109], v[218:221], v[78:81]
	v_mfma_f32_16x16x32_bf16 v[162:165], v[98:101], v[170:173], v[162:165]
	v_mfma_f32_16x16x32_bf16 v[158:161], v[122:125], v[170:173], v[158:161]
	v_mfma_f32_16x16x32_bf16 v[134:137], v[98:101], v[178:181], v[134:137]
	v_mfma_f32_16x16x32_bf16 v[130:133], v[122:125], v[178:181], v[130:133]
	v_mfma_f32_16x16x32_bf16 v[110:113], v[98:101], v[186:189], v[110:113]
	v_mfma_f32_16x16x32_bf16 v[102:105], v[122:125], v[186:189], v[102:105]
	v_mfma_f32_16x16x32_bf16 v[82:85], v[98:101], v[234:237], v[82:85]
	v_mfma_f32_16x16x32_bf16 v[78:81], v[122:125], v[234:237], v[78:81]
	s_setprio 0
	s_setprio 1
	v_mfma_f32_16x16x32_bf16 v[146:149], v[126:129], v[166:169], v[146:149]
	v_mfma_f32_16x16x32_bf16 v[138:141], v[150:153], v[166:169], v[138:141]
	v_mfma_f32_16x16x32_bf16 v[118:121], v[126:129], v[174:177], v[118:121]
	v_mfma_f32_16x16x32_bf16 v[114:117], v[150:153], v[174:177], v[114:117]
	v_mfma_f32_16x16x32_bf16 v[94:97], v[126:129], v[182:185], v[94:97]
	v_mfma_f32_16x16x32_bf16 v[90:93], v[150:153], v[182:185], v[90:93]
	v_mfma_f32_16x16x32_bf16 v[70:73], v[126:129], v[218:221], v[70:73]
	v_mfma_f32_16x16x32_bf16 v[66:69], v[150:153], v[218:221], v[66:69]
	v_mfma_f32_16x16x32_bf16 v[146:149], v[142:145], v[170:173], v[146:149]
	v_mfma_f32_16x16x32_bf16 v[138:141], v[154:157], v[170:173], v[138:141]
	v_mfma_f32_16x16x32_bf16 v[118:121], v[142:145], v[178:181], v[118:121]
	v_mfma_f32_16x16x32_bf16 v[114:117], v[154:157], v[178:181], v[114:117]
	v_mfma_f32_16x16x32_bf16 v[94:97], v[142:145], v[186:189], v[94:97]
	v_mfma_f32_16x16x32_bf16 v[90:93], v[154:157], v[186:189], v[90:93]
	v_mfma_f32_16x16x32_bf16 v[70:73], v[142:145], v[234:237], v[70:73]
	v_mfma_f32_16x16x32_bf16 v[66:69], v[154:157], v[234:237], v[66:69]
	s_setprio 0
	s_barrier
; #define PG8_STAGE(bufoff, gbase, voff) do { _Pragma("unroll") for (int _i = 0; _i < 2; ++_i) \
;         __builtin_amdgcn_global_load_lds((const unsigned*)((const char*)(gbase) + (voff)[_i]), (PG8_LAS unsigned*)(lds + (bufoff) + ldsw + _i * 8192), 16, 0, 0); } while (0)
; #define PG8_LDA(dst, b, h) do { _Pragma("unroll") for (int m = 0; m < 4; ++m) _Pragma("unroll") for (int k = 0; k < 2; ++k) dst[m][k] = *(const PG8_LAS bf16x8*)(lds + PG8_SA(b, h) + aoff + m * 2048 + k * 1024); } while (0)
; #define PG8_MMA(ai, bj, At, Bt) do { __builtin_amdgcn_s_setprio(1); _Pragma("unroll") for (int m = 0; m < 4; ++m) _Pragma("unroll") for (int n = 0; n < 2; ++n) _Pragma("unroll") for (int k = 0; k < 2; ++k) \
;         acc[ai][bj][m][n] = __builtin_amdgcn_mfma_f32_16x16x32_bf16(Bt[n][k], At[m][k], acc[ai][bj][m][n], 0, 0, 0); __builtin_amdgcn_s_setprio(0); } while (0)
; #define PG8_WAIT_V(n) asm volatile("s_waitcnt vmcnt(" #n ")" ::: "memory")
; #define PG8_WAIT_L(n) asm volatile("s_waitcnt lgkmcnt(" #n ")" ::: "memory")
; #define PG8_BAR __builtin_amdgcn_s_barrier()
; #define PG8_SCHED __builtin_amdgcn_sched_barrier(0)
; template <class Epi, class Sched, bool ALIGN_EPI = false, bool SP2 = false>
; __device__ __forceinline__ void gemm_phase(PG8_LAS unsigned char* lds, const Gemm g, const Sched& S, const Epi& E, const int tid) {
;     ...
;         for (int t = 0; t < nt; t += 2) {
;             const bool last = (t == nt - 2);
;             const char* a1 = cA + PG8_KOFFA(t + 1);
;             const char* a2 = last ? nA : cA + PG8_KOFFA(t + 2); const char* b2 = last ? nB : cB + (size_t)(t + 2) * kstep;
;             const char* a3 = a2 + kstep; const char* b3 = b2 + kstep;
;     ...
;             PG8_LDA(At, 1, 1); PG8_STAGE(PG8_SB(1, 0), b3, voffB); PG8_STAGE(PG8_SB(1, 1), b3 + hstep, voffB); PG8_STAGE(PG8_SA(1, 0), a3, voffA);
;             PG8_WAIT_V(8); PG8_WAIT_L(0); PG8_BAR; PG8_MMA(1, 0, At, B0); PG8_MMA(1, 1, At, B1); PG8_BAR; PG8_SCHED;
	s_mov_b32 m0, s54
	v_lshl_add_u64 v[190:191], v[190:191], 0, s[86:87]
	ds_read_b128 v[166:169], v208 offset:49152
	ds_read_b128 v[170:173], v208 offset:50176
	ds_read_b128 v[174:177], v208 offset:51200
	ds_read_b128 v[178:181], v208 offset:52224
	ds_read_b128 v[182:185], v208 offset:53248
	ds_read_b128 v[186:189], v208 offset:54272
	ds_read_b128 v[218:221], v208 offset:55296
	ds_read_b128 v[234:237], v208 offset:56320
	global_load_lds_dwordx4 v[190:191], off
	v_lshl_add_u64 v[190:191], v[222:223], 0, s[86:87]
	s_mov_b32 m0, s55
	s_nop 0
	global_load_lds_dwordx4 v[190:191], off
	v_lshl_add_u64 v[190:191], v[228:229], 0, s[86:87]
	s_mov_b32 m0, s58
	s_nop 0
	global_load_lds_dwordx4 v[190:191], off
	v_lshl_add_u64 v[190:191], v[240:241], 0, s[86:87]
	s_mov_b32 m0, s59
	s_nop 0
	global_load_lds_dwordx4 v[190:191], off
	v_lshl_add_u64 v[190:191], v[242:243], 0, s[86:87]
	s_mov_b32 m0, s56
	s_nop 0
	global_load_lds_dwordx4 v[190:191], off
	v_lshl_add_u64 v[190:191], v[244:245], 0, s[86:87]
	s_mov_b32 m0, s57
	s_nop 0
	global_load_lds_dwordx4 v[190:191], off
	s_waitcnt vmcnt(8)
	s_waitcnt lgkmcnt(0)
	s_barrier
	s_setprio 1
	s_waitcnt lgkmcnt(0)
	v_mfma_f32_16x16x32_bf16 v[62:65], v[86:89], v[166:169], v[62:65]
	v_mfma_f32_16x16x32_bf16 v[58:61], v[106:109], v[166:169], v[58:61]
	v_mfma_f32_16x16x32_bf16 v[46:49], v[86:89], v[174:177], v[46:49]
	v_mfma_f32_16x16x32_bf16 v[42:45], v[106:109], v[174:177], v[42:45]
	v_mfma_f32_16x16x32_bf16 v[30:33], v[86:89], v[182:185], v[30:33]
	v_mfma_f32_16x16x32_bf16 v[26:29], v[106:109], v[182:185], v[26:29]
	v_mfma_f32_16x16x32_bf16 v[14:17], v[86:89], v[218:221], v[14:17]
	v_mfma_f32_16x16x32_bf16 v[10:13], v[106:109], v[218:221], v[10:13]
	v_mfma_f32_16x16x32_bf16 v[62:65], v[98:101], v[170:173], v[62:65]
	v_mfma_f32_16x16x32_bf16 v[58:61], v[122:125], v[170:173], v[58:61]
	v_mfma_f32_16x16x32_bf16 v[46:49], v[98:101], v[178:181], v[46:49]
	v_mfma_f32_16x16x32_bf16 v[42:45], v[122:125], v[178:181], v[42:45]
	v_mfma_f32_16x16x32_bf16 v[30:33], v[98:101], v[186:189], v[30:33]
	v_mfma_f32_16x16x32_bf16 v[26:29], v[122:125], v[186:189], v[26:29]
	v_mfma_f32_16x16x32_bf16 v[14:17], v[98:101], v[234:237], v[14:17]
	v_mfma_f32_16x16x32_bf16 v[10:13], v[122:125], v[234:237], v[10:13]
	s_setprio 0
	s_setprio 1
	v_mfma_f32_16x16x32_bf16 v[54:57], v[126:129], v[166:169], v[54:57]
	v_mfma_f32_16x16x32_bf16 v[50:53], v[150:153], v[166:169], v[50:53]
	v_mfma_f32_16x16x32_bf16 v[38:41], v[126:129], v[174:177], v[38:41]
	v_mfma_f32_16x16x32_bf16 v[34:37], v[150:153], v[174:177], v[34:37]
	v_mfma_f32_16x16x32_bf16 v[22:25], v[126:129], v[182:185], v[22:25]
	v_mfma_f32_16x16x32_bf16 v[18:21], v[150:153], v[182:185], v[18:21]
	v_mfma_f32_16x16x32_bf16 v[6:9], v[126:129], v[218:221], v[6:9]
	v_mfma_f32_16x16x32_bf16 v[2:5], v[150:153], v[218:221], v[2:5]
	v_mfma_f32_16x16x32_bf16 v[54:57], v[142:145], v[170:173], v[54:57]
	v_mfma_f32_16x16x32_bf16 v[50:53], v[154:157], v[170:173], v[50:53]
	v_mfma_f32_16x16x32_bf16 v[38:41], v[142:145], v[178:181], v[38:41]
	v_mfma_f32_16x16x32_bf16 v[34:37], v[154:157], v[178:181], v[34:37]
	v_mfma_f32_16x16x32_bf16 v[22:25], v[142:145], v[186:189], v[22:25]
	v_mfma_f32_16x16x32_bf16 v[18:21], v[154:157], v[186:189], v[18:21]
	v_mfma_f32_16x16x32_bf16 v[6:9], v[142:145], v[234:237], v[6:9]
	v_mfma_f32_16x16x32_bf16 v[2:5], v[154:157], v[234:237], v[2:5]
	s_setprio 0
	s_barrier
	s_add_u32 s26, s26, 2
	s_addc_u32 s27, s27, 0
	s_add_i32 s38, s26, -2
	s_add_u32 s30, s30, 0x100
	s_addc_u32 s31, s31, 0
	s_add_u32 s28, s28, 2
	s_addc_u32 s29, s29, 0
	s_cmp_ge_u32 s38, s61
	s_cbranch_scc1 .LBB0_419
.LBB0_417:
	v_or_b32_e32 v0, 0x10000, v209
	v_add_u32_e32 v98, 0x10400, v209
	ds_read_b128 v[86:89], v0
	ds_read_b128 v[98:101], v98
	v_add_u32_e32 v0, 0x10800, v209
	v_add_u32_e32 v122, 0x10c00, v209
	ds_read_b128 v[106:109], v0
	ds_read_b128 v[122:125], v122
	v_or_b32_e32 v0, 0x14000, v209
	v_add_u32_e32 v142, 0x14400, v209
	ds_read_b128 v[126:129], v0
	ds_read_b128 v[142:145], v142
	v_add_u32_e32 v0, 0x14800, v209
	v_add_u32_e32 v154, 0x14c00, v209
	ds_read_b128 v[150:153], v0
	ds_read_b128 v[154:157], v154
	s_cmp_eq_u32 s61, s26
	s_cselect_b64 s[40:41], -1, 0
	s_and_b64 vcc, exec, s[40:41]
	s_mov_b64 s[38:39], s[24:25]
	s_cbranch_vccnz .LBB0_416
	s_lshr_b64 s[38:39], s[26:27], 4
	s_lshr_b32 s39, s27, 4
	s_mul_i32 s39, s39, 0x7ff800
	s_mul_hi_u32 s68, s38, 0x7ff800
	s_add_i32 s68, s68, s39
	s_mul_i32 s38, s38, 0x7ff800
	s_add_u32 s38, s66, s38
	s_addc_u32 s39, s67, s68
	s_add_u32 s38, s38, s30
	s_addc_u32 s39, s39, s31
	s_branch .LBB0_416
